# speedup vs baseline: 1.0143x; 1.0031x over previous
_Z11prep_kernel8PrepArgs:
	v_lshrrev_b32_e32 v66, 6, v0
	v_mov_b32_e32 v1, 0
	v_mov_b32_e32 v172, 0
	v_and_b32_e32 v67, 63, v0
	v_cmp_eq_u32_e64 s[8:9], 5, v66
	s_and_saveexec_b64 s[4:5], s[8:9]
	s_cbranch_execz .LBB1_2
	s_getpc_b64 s[6:7]
	s_and_b32 s6, s6, 0xffffff80
	v_lshlrev_b32_e32 v2, 7, v67
	v_mov_b32_e32 v3, 0
	v_lshl_add_u64 v[2:3], s[6:7], 0, v[2:3]
	v_add_co_u32_e32 v4, vcc, 0x2000, v2
	s_nop 1
	v_addc_co_u32_e32 v5, vcc, 0, v3, vcc
	v_add_co_u32_e32 v6, vcc, 0x4000, v2
	s_nop 1
	v_addc_co_u32_e32 v7, vcc, 0, v3, vcc
	v_add_co_u32_e32 v8, vcc, 0x6000, v2
	s_nop 1
	v_addc_co_u32_e32 v9, vcc, 0, v3, vcc
	global_load_dword v250, v[2:3], off
	global_load_dword v251, v[4:5], off
	global_load_dword v252, v[6:7], off
	global_load_dword v253, v[8:9], off
